# P0 H8 stores nt
# baseline (speedup 1.0000x reference)
.LBB0_85:
	s_ashr_i32 s1, s0, 31
	s_lshl_b64 s[2:3], s[0:1], 12
	v_lshl_add_u64 v[18:19], v[42:43], 0, s[2:3]
	s_add_i32 s6, s0, s5
	global_load_dwordx4 v[56:59], v[18:19], off nt
	global_load_dwordx4 v[34:37], v[18:19], off offset:1024 nt
	global_load_dwordx4 v[26:29], v[18:19], off offset:2048 nt
	s_ashr_i32 s7, s6, 31
	global_load_dwordx4 v[18:21], v[18:19], off offset:3072 nt
	s_lshl_b64 s[2:3], s[6:7], 12
	v_lshl_add_u64 v[22:23], v[42:43], 0, s[2:3]
	global_load_dwordx4 v[60:63], v[22:23], off nt
	global_load_dwordx4 v[38:41], v[22:23], off offset:1024 nt
	global_load_dwordx4 v[30:33], v[22:23], off offset:2048 nt
	s_nop 0
	global_load_dwordx4 v[22:25], v[22:23], off offset:3072 nt
	s_lshl_b64 s[8:9], s[0:1], 10
	s_lshl_b64 s[10:11], s[6:7], 10
	s_waitcnt vmcnt(7)
	v_mul_f32_e32 v55, v57, v57
	v_mul_f32_e32 v64, v59, v59
	s_waitcnt vmcnt(6)
	v_mul_f32_e32 v65, v35, v35
	v_mul_f32_e32 v67, v37, v37
	s_waitcnt vmcnt(5)
	v_mul_f32_e32 v70, v27, v27
	v_mul_f32_e32 v71, v29, v29
	v_fmac_f32_e32 v55, v56, v56
	v_fmac_f32_e32 v64, v58, v58
	v_fmac_f32_e32 v65, v34, v34
	v_fmac_f32_e32 v67, v36, v36
	s_waitcnt vmcnt(4)
	v_mul_f32_e32 v72, v19, v19
	v_mul_f32_e32 v73, v21, v21
	s_waitcnt vmcnt(3)
	v_mul_f32_e32 v74, v61, v61
	v_mul_f32_e32 v75, v63, v63
	s_waitcnt vmcnt(2)
	v_mul_f32_e32 v76, v39, v39
	v_mul_f32_e32 v77, v41, v41
	v_fmac_f32_e32 v70, v26, v26
	v_fmac_f32_e32 v71, v28, v28
	v_add_f32_e32 v55, v55, v64
	v_add_f32_e32 v64, v65, v67
	s_waitcnt vmcnt(1)
	v_mul_f32_e32 v78, v31, v31
	v_mul_f32_e32 v79, v33, v33
	v_fmac_f32_e32 v72, v18, v18
	v_fmac_f32_e32 v73, v20, v20
	v_fmac_f32_e32 v74, v60, v60
	v_fmac_f32_e32 v75, v62, v62
	v_fmac_f32_e32 v76, v38, v38
	v_fmac_f32_e32 v77, v40, v40
	v_add_f32_e32 v65, v70, v71
	v_add_f32_e32 v55, v55, v64
	s_waitcnt vmcnt(0)
	v_mul_f32_e32 v80, v23, v23
	v_mul_f32_e32 v81, v25, v25
	v_fmac_f32_e32 v78, v30, v30
	v_fmac_f32_e32 v79, v32, v32
	v_add_f32_e32 v67, v72, v73
	v_add_f32_e32 v70, v74, v75
	v_add_f32_e32 v64, v76, v77
	v_add_f32_e32 v55, v55, v65
	v_fmac_f32_e32 v80, v22, v22
	v_fmac_f32_e32 v81, v24, v24
	v_add_f32_e32 v71, v78, v79
	v_add_f32_e32 v64, v70, v64
	v_add_f32_e32 v55, v55, v67
	v_add_f32_e32 v72, v80, v81
	v_add_f32_e32 v64, v64, v71
	ds_bpermute_b32 v65, v46, v55
	v_add_f32_e32 v64, v64, v72
	ds_bpermute_b32 v67, v46, v64
	s_waitcnt lgkmcnt(1)
	v_add_f32_e32 v55, v55, v65
	ds_bpermute_b32 v65, v47, v55
	s_waitcnt lgkmcnt(1)
	v_add_f32_e32 v64, v64, v67
	ds_bpermute_b32 v67, v47, v64
	s_waitcnt lgkmcnt(1)
	v_add_f32_e32 v55, v55, v65
	ds_bpermute_b32 v65, v48, v55
	s_waitcnt lgkmcnt(1)
	v_add_f32_e32 v64, v64, v67
	ds_bpermute_b32 v67, v48, v64
	s_waitcnt lgkmcnt(1)
	v_add_f32_e32 v55, v55, v65
	ds_bpermute_b32 v65, v49, v55
	s_waitcnt lgkmcnt(1)
	v_add_f32_e32 v64, v64, v67
	ds_bpermute_b32 v67, v49, v64
	s_waitcnt lgkmcnt(1)
	v_add_f32_e32 v55, v55, v65
	ds_bpermute_b32 v65, v50, v55
	s_waitcnt lgkmcnt(1)
	v_add_f32_e32 v64, v64, v67
	ds_bpermute_b32 v67, v50, v64
	s_waitcnt lgkmcnt(1)
	v_add_f32_e32 v55, v55, v65
	ds_bpermute_b32 v65, v51, v55
	s_waitcnt lgkmcnt(1)
	v_add_f32_e32 v64, v64, v67
	ds_bpermute_b32 v67, v51, v64
	s_waitcnt lgkmcnt(1)
	v_add_f32_e32 v55, v55, v65
	v_fmamk_f32 v55, v55, 0x3a800000, v52
	s_waitcnt lgkmcnt(0)
	v_add_f32_e32 v64, v64, v67
	v_mul_f32_e32 v65, 0x4f800000, v55
	v_cmp_gt_f32_e32 vcc, s12, v55
	v_fmamk_f32 v64, v64, 0x3a800000, v52
	v_cmp_gt_f32_e64 s[0:1], s12, v64
	v_cndmask_b32_e32 v55, v55, v65, vcc
	v_mul_f32_e32 v65, 0x4f800000, v64
	v_sqrt_f32_e32 v67, v55
	v_cndmask_b32_e64 v64, v64, v65, s[0:1]
	v_sqrt_f32_e32 v65, v64
	v_add_u32_e32 v70, -1, v67
	v_add_u32_e32 v71, 1, v67
	v_fma_f32 v72, -v70, v67, v55
	v_fma_f32 v73, -v71, v67, v55
	v_add_u32_e32 v74, -1, v65
	v_cmp_ge_f32_e64 s[2:3], 0, v72
	v_add_u32_e32 v75, 1, v65
	v_fma_f32 v72, -v75, v65, v64
	v_cndmask_b32_e64 v67, v67, v70, s[2:3]
	v_fma_f32 v70, -v74, v65, v64
	v_cmp_lt_f32_e64 s[2:3], 0, v73
	s_nop 1
	v_cndmask_b32_e64 v67, v67, v71, s[2:3]
	v_cmp_ge_f32_e64 s[2:3], 0, v70
	v_mul_f32_e32 v70, 0x37800000, v67
	v_cndmask_b32_e32 v67, v67, v70, vcc
	v_cndmask_b32_e64 v65, v65, v74, s[2:3]
	v_cmp_lt_f32_e64 s[2:3], 0, v72
	v_cmp_class_f32_e32 vcc, v55, v53
	s_nop 0
	v_cndmask_b32_e64 v65, v65, v75, s[2:3]
	v_mul_f32_e32 v70, 0x37800000, v65
	v_cndmask_b32_e32 v55, v67, v55, vcc
	v_cndmask_b32_e64 v65, v65, v70, s[0:1]
	v_div_scale_f32 v67, s[0:1], v55, v55, 1.0
	v_cmp_class_f32_e64 s[0:1], v64, v53
	v_div_scale_f32 v70, vcc, 1.0, v55, 1.0
	s_nop 0
	v_cndmask_b32_e64 v64, v65, v64, s[0:1]
	v_rcp_f32_e32 v65, v67
	v_div_scale_f32 v71, s[0:1], v64, v64, 1.0
	v_rcp_f32_e32 v72, v71
	v_fma_f32 v74, -v67, v65, 1.0
	v_fmac_f32_e32 v65, v74, v65
	v_div_scale_f32 v73, s[0:1], 1.0, v64, 1.0
	v_fma_f32 v74, -v71, v72, 1.0
	v_mul_f32_e32 v75, v70, v65
	v_fmac_f32_e32 v72, v74, v72
	v_fma_f32 v74, -v67, v75, v70
	v_mul_f32_e32 v76, v73, v72
	v_fmac_f32_e32 v75, v74, v65
	v_fma_f32 v74, -v71, v76, v73
	v_fma_f32 v67, -v67, v75, v70
	v_fmac_f32_e32 v76, v74, v72
	v_div_fmas_f32 v65, v67, v65, v75
	v_fma_f32 v67, -v71, v76, v73
	s_mov_b64 vcc, s[0:1]
	v_div_fixup_f32 v55, v65, v55, 1.0
	v_div_fmas_f32 v65, v67, v72, v76
	v_div_fixup_f32 v65, v65, v64, 1.0
	v_mul_f32_e32 v64, 0x41800000, v55
	v_pk_mul_f32 v[56:57], v[56:57], v[64:65] op_sel_hi:[1,0]
	v_mul_f32_e32 v70, 0x41800000, v65
	v_pk_mul_f32 v[56:57], v[2:3], v[56:57]
	v_pk_mul_f32 v[58:59], v[58:59], v[64:65] op_sel_hi:[1,0]
	v_med3_f32 v55, v56, s13, v54
	v_med3_f32 v56, v57, s13, v54
	v_mov_b32_e32 v65, 0
	v_cvt_pk_fp8_f32 v65, v55, v56
	v_pk_mul_f32 v[58:59], v[4:5], v[58:59]
	v_pk_mul_f32 v[60:61], v[60:61], v[70:71] op_sel_hi:[1,0]
	v_med3_f32 v55, v58, s13, v54
	v_med3_f32 v56, v59, s13, v54
	v_pk_mul_f32 v[60:61], v[2:3], v[60:61]
	v_cvt_pk_fp8_f32 v65, v55, v56 op_sel:[0,0,1]
	v_med3_f32 v57, v60, s13, v54
	v_med3_f32 v58, v61, s13, v54
	v_mov_b32_e32 v60, 0
	v_cvt_pk_fp8_f32 v60, v57, v58
	v_pk_mul_f32 v[62:63], v[62:63], v[70:71] op_sel_hi:[1,0]
	v_pk_mul_f32 v[34:35], v[34:35], v[64:65] op_sel_hi:[1,0]
	v_pk_mul_f32 v[62:63], v[4:5], v[62:63]
	v_pk_mul_f32 v[36:37], v[36:37], v[64:65] op_sel_hi:[1,0]
	v_med3_f32 v55, v62, s13, v54
	v_med3_f32 v56, v63, s13, v54
	v_pk_mul_f32 v[34:35], v[6:7], v[34:35]
	v_pk_mul_f32 v[38:39], v[38:39], v[70:71] op_sel_hi:[1,0]
	v_cvt_pk_fp8_f32 v60, v55, v56 op_sel:[0,0,1]
	v_pk_mul_f32 v[36:37], v[8:9], v[36:37]
	v_pk_mul_f32 v[38:39], v[6:7], v[38:39]
	v_med3_f32 v34, v34, s13, v54
	v_med3_f32 v35, v35, s13, v54
	v_mov_b32_e32 v55, 0
	v_cvt_pk_fp8_f32 v55, v34, v35
	v_med3_f32 v34, v36, s13, v54
	v_med3_f32 v35, v37, s13, v54
	v_med3_f32 v36, v38, s13, v54
	v_med3_f32 v37, v39, s13, v54
	v_mov_b32_e32 v38, 0
	v_cvt_pk_fp8_f32 v38, v36, v37
	v_pk_mul_f32 v[40:41], v[40:41], v[70:71] op_sel_hi:[1,0]
	v_pk_mul_f32 v[26:27], v[26:27], v[64:65] op_sel_hi:[1,0]
	v_pk_mul_f32 v[40:41], v[8:9], v[40:41]
	v_cvt_pk_fp8_f32 v55, v34, v35 op_sel:[0,0,1]
	v_med3_f32 v34, v40, s13, v54
	v_med3_f32 v35, v41, s13, v54
	v_pk_mul_f32 v[28:29], v[28:29], v[64:65] op_sel_hi:[1,0]
	v_pk_mul_f32 v[26:27], v[10:11], v[26:27]
	v_pk_mul_f32 v[30:31], v[30:31], v[70:71] op_sel_hi:[1,0]
	v_cvt_pk_fp8_f32 v38, v34, v35 op_sel:[0,0,1]
	v_pk_mul_f32 v[28:29], v[12:13], v[28:29]
	v_pk_mul_f32 v[30:31], v[10:11], v[30:31]
	v_med3_f32 v26, v26, s13, v54
	v_med3_f32 v27, v27, s13, v54
	v_mov_b32_e32 v34, 0
	v_cvt_pk_fp8_f32 v34, v26, v27
	v_med3_f32 v26, v28, s13, v54
	v_med3_f32 v27, v29, s13, v54
	v_med3_f32 v28, v30, s13, v54
	v_med3_f32 v29, v31, s13, v54
	v_mov_b32_e32 v30, 0
	v_cvt_pk_fp8_f32 v30, v28, v29
	v_pk_mul_f32 v[32:33], v[32:33], v[70:71] op_sel_hi:[1,0]
	v_pk_mul_f32 v[18:19], v[18:19], v[64:65] op_sel_hi:[1,0]
	v_pk_mul_f32 v[32:33], v[12:13], v[32:33]
	v_cvt_pk_fp8_f32 v34, v26, v27 op_sel:[0,0,1]
	v_med3_f32 v26, v32, s13, v54
	v_med3_f32 v27, v33, s13, v54
	v_pk_mul_f32 v[20:21], v[20:21], v[64:65] op_sel_hi:[1,0]
	v_pk_mul_f32 v[18:19], v[14:15], v[18:19]
	v_pk_mul_f32 v[22:23], v[22:23], v[70:71] op_sel_hi:[1,0]
	v_cvt_pk_fp8_f32 v30, v26, v27 op_sel:[0,0,1]
	v_pk_mul_f32 v[20:21], v[16:17], v[20:21]
	v_pk_mul_f32 v[22:23], v[14:15], v[22:23]
	v_med3_f32 v18, v18, s13, v54
	v_med3_f32 v19, v19, s13, v54
	v_mov_b32_e32 v26, 0
	v_cvt_pk_fp8_f32 v26, v18, v19
	v_med3_f32 v18, v20, s13, v54
	v_med3_f32 v19, v21, s13, v54
	v_med3_f32 v20, v22, s13, v54
	v_med3_f32 v21, v23, s13, v54
	v_mov_b32_e32 v22, 0
	v_cvt_pk_fp8_f32 v22, v20, v21
	v_pk_mul_f32 v[24:25], v[24:25], v[70:71] op_sel_hi:[1,0]
	v_cvt_pk_fp8_f32 v26, v18, v19 op_sel:[0,0,1]
	v_pk_mul_f32 v[24:25], v[16:17], v[24:25]
	s_add_i32 s0, s6, s5
	v_med3_f32 v18, v24, s13, v54
	v_med3_f32 v19, v25, s13, v54
	v_cvt_pk_fp8_f32 v22, v18, v19 op_sel:[0,0,1]
	v_lshl_add_u64 v[56:57], v[44:45], 0, s[8:9]
	v_lshl_add_u64 v[58:59], v[44:45], 0, s[10:11]
	s_cmpk_gt_i32 s0, 0x7fff
	global_store_dword v[56:57], v65, off nt
	global_store_dword v[58:59], v60, off nt
	global_store_dword v[56:57], v55, off offset:256 nt
	global_store_dword v[58:59], v38, off offset:256 nt
	global_store_dword v[56:57], v34, off offset:512 nt
	global_store_dword v[58:59], v30, off offset:512 nt
	global_store_dword v[56:57], v26, off offset:768 nt
	global_store_dword v[58:59], v22, off offset:768 nt
	s_cbranch_scc0 .LBB0_85
